# v35 + indexer-score head loops rotated: next iteration's key-fragment ds_reads issued right after the MFMAs (2 fresh quads + 2 dedicated buffers), drain after loop
# speedup vs baseline: 1.0110x; 1.0033x over previous
; __device__ __forceinline__ unsigned ordkey(float f) { const unsigned u = __float_as_uint(f); return u ^ ((unsigned)((int)u >> 31) | 0x80000000u); }
; __device__ __forceinline__ int crow(int r, int hi) { return (r & 3) + 8 * (r >> 2) + 4 * hi; }
; __global__ void __launch_bounds__(NWAVES * 64, 2) mega_fwd(Args args) {
;     ...
;               unsigned sgnbits = 0u;
; #pragma unroll
;               for (int h = 0; h < 8; ++h) sgnbits |= ((float)iwv[h] < 0.f) ? (1u << h) : 0u;
;     ...
;               for (int ti = 0; ti < 4; ++ti) { const int kt = F.wave + 8 * ti;
;                 if (kt < ntiles) { const int k0 = 64 * kt;
; #pragma unroll
;                     for (int half = 0; half < 2; ++half) { const f16x8 kf0 = kfr[ti][half][0], kf1 = kfr[ti][half][1];
;                         fa::f32x16 sc;
; #pragma unroll
;                         for (int r = 0; r < 16; ++r) sc[r] = 0.f;
;                         sc = __builtin_amdgcn_mfma_f32_32x32x16_f16(kf0, __builtin_bit_cast(f16x8, iqL[16 * 64 + lane]), sc, 0, 0, 0);
;                         sc = __builtin_amdgcn_mfma_f32_32x32x16_f16(kf1, __builtin_bit_cast(f16x8, iqL[17 * 64 + lane]), sc, 0, 0, 0);
; #pragma unroll 2
;                         for (int h = 0; h < 8; ++h) { fa::f32x16 a;
; #pragma unroll
;                             for (int r = 0; r < 16; ++r) a[r] = 0.f;
;                             a = __builtin_amdgcn_mfma_f32_32x32x16_f16(kf0, __builtin_bit_cast(f16x8, iqL[(2 * h) * 64 + lane]), a, 0, 0, 0);
;                             a = __builtin_amdgcn_mfma_f32_32x32x16_f16(kf1, __builtin_bit_cast(f16x8, iqL[(2 * h + 1) * 64 + lane]), a, 0, 0, 0);
;                             const float sg = ((sgnbits >> h) & 1u) ? -1.f : 1.f;
; #pragma unroll
;                             for (int r = 0; r < 16; ++r) sc[r] = __builtin_fmaf(__builtin_fabsf(a[r]), sg, sc[r]); }
; #pragma unroll
;                         for (int r = 0; r < 16; ++r) keys[ti][16 * half + r] = ordkey(sc[r]);
;                         if (k0 + 63 > 32 * qg) {
; #pragma unroll
;                             for (int r = 0; r < 16; ++r) { const int kidx = k0 + 32 * half + fa::crow(r, hi); keys[ti][16 * half + r] = (kidx <= t) ? keys[ti][16 * half + r] : 0u; } } }
.LBB0_619:
	v_cmp_gt_f16_e32 vcc, 0, v3
	v_cmp_lt_f16_sdwa s[40:41], v2, v1 src0_sel:WORD_1 src1_sel:DWORD
	s_mov_b32 s26, 0
	v_cndmask_b32_e64 v7, 0, 4, vcc
	v_cmp_gt_f16_e32 vcc, 0, v4
	v_cndmask_b32_e64 v6, 0, 2, s[40:41]
	v_cmp_lt_f16_sdwa s[40:41], v3, v1 src0_sel:WORD_1 src1_sel:DWORD
	v_cndmask_b32_e64 v8, 0, 16, vcc
	v_cmp_gt_f16_e32 vcc, 0, v5
	v_cndmask_b32_e64 v3, 0, 8, s[40:41]
	v_cmp_lt_f16_sdwa s[40:41], v4, v1 src0_sel:WORD_1 src1_sel:DWORD
	v_cndmask_b32_e64 v9, 0, 64, vcc
	v_cmp_lt_f16_sdwa vcc, v5, v1 src0_sel:WORD_1 src1_sel:DWORD
	v_cndmask_b32_e64 v4, 0, 32, s[40:41]
	v_lshlrev_b32_e32 v142, 2, v104
	v_cndmask_b32_e32 v5, 0, v245, vcc
	v_cmp_gt_f16_e32 vcc, 0, v2
	s_waitcnt lgkmcnt(0)
	s_barrier
	v_cndmask_b32_e64 v2, 0, 1, vcc
	v_or_b32_e32 v2, v6, v2
	v_or3_b32 v2, v7, v2, v3
	v_or3_b32 v2, v8, v2, v4
	v_or3_b32 v140, v9, v2, v5
	v_mov_b32_e32 v2, 0xb000
	v_lshl_add_u32 v141, v112, 4, v2
	s_and_b64 vcc, exec, s[38:39]
	s_cbranch_vccnz .LBB0_655
	ds_read_b128 v[106:109], v141 offset:16384
	ds_read_b128 v[102:105], v141 offset:17408
	v_mov_b32_e32 v52, v141
	s_waitcnt lgkmcnt(1)
	v_mfma_f32_32x32x16_f16 v[2:17], v[46:49], v[106:109], 0
	s_waitcnt lgkmcnt(0)
	v_mfma_f32_32x32x16_f16 v[2:17], v[42:45], v[102:105], v[2:17]
	s_nop 11
	v_mov_b32_e32 v51, v2
	v_mov_b32_e32 v2, v3
	v_mov_b32_e32 v50, v4
	v_mov_b32_e32 v3, v5
	ds_read_b128 v[172:175], v52
	ds_read_b128 v[196:199], v52 offset:1024
	ds_read_b128 v[224:227], v52 offset:2048
	ds_read_b128 v[176:179], v52 offset:3072
.LBB0_621:
	s_waitcnt lgkmcnt(3)
	v_mfma_f32_32x32x16_f16 v[18:33], v[46:49], v[172:175], 0
	s_waitcnt lgkmcnt(2)
	v_mfma_f32_32x32x16_f16 v[18:33], v[42:45], v[196:199], v[18:33]
	s_waitcnt lgkmcnt(1)
	v_mfma_f32_32x32x16_f16 v[208:223], v[46:49], v[224:227], 0
	s_waitcnt lgkmcnt(0)
	v_mfma_f32_32x32x16_f16 v[208:223], v[42:45], v[176:179], v[208:223]
	v_add_u32_e32 v52, 0x1000, v52
	ds_read_b128 v[172:175], v52
	ds_read_b128 v[196:199], v52 offset:1024
	ds_read_b128 v[224:227], v52 offset:2048
	ds_read_b128 v[176:179], v52 offset:3072
	v_bfe_u32 v4, v140, s26, 1
	v_cmp_eq_u32_e32 vcc, 0, v4
	v_lshrrev_b32_e32 v180, s26, v140
	v_and_b32_e32 v180, 2, v180
	v_cndmask_b32_e64 v4, -1.0, 1.0, vcc
	v_cmp_eq_u32_e32 vcc, 0, v180
	s_add_i32 s26, s26, 2
	v_cndmask_b32_e64 v180, -1.0, 1.0, vcc
	s_cmp_eq_u32 s26, 8
	v_fma_f32 v50, |v20|, v4, v50
	v_fma_f32 v51, |v18|, v4, v51
	v_fma_f32 v114, |v19|, v4, v2
	v_fma_f32 v115, |v21|, v4, v3
	v_fma_f32 v22, |v22|, v4, v6
	v_fma_f32 v23, |v23|, v4, v7
	v_fma_f32 v24, |v24|, v4, v8
	v_fma_f32 v25, |v25|, v4, v9
	v_fma_f32 v26, |v26|, v4, v10
	v_fma_f32 v27, |v27|, v4, v11
	v_fma_f32 v28, |v28|, v4, v12
	v_fma_f32 v29, |v29|, v4, v13
	v_fma_f32 v30, |v30|, v4, v14
	v_fma_f32 v31, |v31|, v4, v15
	v_fma_f32 v32, |v32|, v4, v16
	v_fma_f32 v33, |v33|, v4, v17
	v_fma_f32 v50, |v210|, v180, v50
	v_fma_f32 v51, |v208|, v180, v51
	v_fma_f32 v2, |v209|, v180, v114
	v_fma_f32 v3, |v211|, v180, v115
	v_fma_f32 v8, |v214|, v180, v24
	v_fma_f32 v9, |v215|, v180, v25
	v_fma_f32 v6, |v212|, v180, v22
	v_fma_f32 v7, |v213|, v180, v23
	v_fma_f32 v12, |v218|, v180, v28
	v_fma_f32 v13, |v219|, v180, v29
	v_fma_f32 v10, |v216|, v180, v26
	v_fma_f32 v11, |v217|, v180, v27
	v_fma_f32 v16, |v222|, v180, v32
	v_fma_f32 v17, |v223|, v180, v33
	v_fma_f32 v14, |v220|, v180, v30
	v_fma_f32 v15, |v221|, v180, v31
	s_cbranch_scc0 .LBB0_621
	s_waitcnt lgkmcnt(0)
	v_ashrrev_i32_e32 v4, 31, v51
	v_ashrrev_i32_e32 v5, 31, v50
	v_or_b32_e32 v4, 0x80000000, v4
	v_or_b32_e32 v5, 0x80000000, v5
	v_xor_b32_e32 v115, v4, v51
	v_xor_b32_e32 v114, v5, v50
	v_ashrrev_i32_e32 v4, 31, v3
	v_ashrrev_i32_e32 v5, 31, v2
	v_or_b32_e32 v4, 0x80000000, v4
	v_or_b32_e32 v5, 0x80000000, v5
	v_readlane_b32 s26, v254, 33
	v_xor_b32_e32 v117, v4, v3
	v_xor_b32_e32 v116, v5, v2
	v_ashrrev_i32_e32 v2, 31, v6
	v_ashrrev_i32_e32 v3, 31, v7
	v_ashrrev_i32_e32 v4, 31, v8
	v_ashrrev_i32_e32 v5, 31, v9
	s_cmp_gt_u32 s26, s44
	v_bitop3_b32 v53, v5, v9, s68 bitop3:0x36
	v_bitop3_b32 v52, v4, v8, s68 bitop3:0x36
	v_bitop3_b32 v51, v3, v7, s68 bitop3:0x36
	v_bitop3_b32 v50, v2, v6, s68 bitop3:0x36
	v_ashrrev_i32_e32 v2, 31, v10
	v_ashrrev_i32_e32 v3, 31, v11
	v_ashrrev_i32_e32 v4, 31, v12
	v_ashrrev_i32_e32 v5, 31, v13
	s_cselect_b64 s[40:41], -1, 0
	v_bitop3_b32 v45, v5, v13, s68 bitop3:0x36
	v_bitop3_b32 v44, v4, v12, s68 bitop3:0x36
	v_bitop3_b32 v43, v3, v11, s68 bitop3:0x36
	v_bitop3_b32 v42, v2, v10, s68 bitop3:0x36
	v_ashrrev_i32_e32 v2, 31, v14
	v_ashrrev_i32_e32 v3, 31, v15
	v_ashrrev_i32_e32 v4, 31, v16
	v_ashrrev_i32_e32 v5, 31, v17
	v_add_u32_e32 v118, s18, v142
	v_bitop3_b32 v49, v5, v17, s68 bitop3:0x36
	v_bitop3_b32 v48, v4, v16, s68 bitop3:0x36
	v_bitop3_b32 v47, v3, v15, s68 bitop3:0x36
	v_bitop3_b32 v46, v2, v14, s68 bitop3:0x36
	s_and_b64 vcc, exec, s[40:41]
	s_cbranch_vccz .LBB0_624
	v_or_b32_e32 v2, 2, v118
	v_cmp_le_i32_e32 vcc, v118, v124
	v_add_u32_e32 v5, 11, v118
	v_add_u32_e32 v4, 10, v118
	v_cndmask_b32_e32 v115, 0, v115, vcc
	v_cmp_le_i32_e32 vcc, v2, v124
	v_or_b32_e32 v2, 3, v118
	v_add_u32_e32 v3, 9, v118
	v_cndmask_b32_e32 v114, 0, v114, vcc
	v_cmp_lt_i32_e32 vcc, v118, v124
	s_nop 1
	v_cndmask_b32_e32 v116, 0, v116, vcc
	v_cmp_ge_i32_e32 vcc, v124, v2
	v_add_u32_e32 v2, 8, v118
	s_nop 0
	v_cndmask_b32_e32 v117, 0, v117, vcc
	v_cmp_le_i32_e32 vcc, v5, v124
	v_add_u32_e32 v5, 19, v118
	s_nop 0
	v_cndmask_b32_e32 v53, 0, v53, vcc
	v_cmp_le_i32_e32 vcc, v4, v124
	v_add_u32_e32 v4, 18, v118
	s_nop 0
	v_cndmask_b32_e32 v52, 0, v52, vcc
	v_cmp_le_i32_e32 vcc, v3, v124
	v_add_u32_e32 v3, 17, v118
	s_nop 0
	v_cndmask_b32_e32 v51, 0, v51, vcc
	v_cmp_le_i32_e32 vcc, v2, v124
	v_add_u32_e32 v2, 16, v118
	s_nop 0
	v_cndmask_b32_e32 v50, 0, v50, vcc
	v_cmp_le_i32_e32 vcc, v5, v124
	v_add_u32_e32 v5, 27, v118
	s_nop 0
	v_cndmask_b32_e32 v45, 0, v45, vcc
	v_cmp_le_i32_e32 vcc, v4, v124
	v_add_u32_e32 v4, 26, v118
	s_nop 0
	v_cndmask_b32_e32 v44, 0, v44, vcc
	v_cmp_le_i32_e32 vcc, v3, v124
	v_add_u32_e32 v3, 25, v118
	s_nop 0
	v_cndmask_b32_e32 v43, 0, v43, vcc
	v_cmp_le_i32_e32 vcc, v2, v124
	v_add_u32_e32 v2, 24, v118
	s_nop 0
	v_cndmask_b32_e32 v42, 0, v42, vcc
	v_cmp_le_i32_e32 vcc, v5, v124
	s_nop 1
	v_cndmask_b32_e32 v49, 0, v49, vcc
	v_cmp_le_i32_e32 vcc, v4, v124
	s_nop 1
	v_cndmask_b32_e32 v48, 0, v48, vcc
	v_cmp_le_i32_e32 vcc, v3, v124
	s_nop 1
	v_cndmask_b32_e32 v47, 0, v47, vcc
	v_cmp_le_i32_e32 vcc, v2, v124
	s_nop 1
	v_cndmask_b32_e32 v46, 0, v46, vcc
; __device__ __forceinline__ unsigned ordkey(float f) { const unsigned u = __float_as_uint(f); return u ^ ((unsigned)((int)u >> 31) | 0x80000000u); }
; __device__ __forceinline__ int crow(int r, int hi) { return (r & 3) + 8 * (r >> 2) + 4 * hi; }
; __global__ void __launch_bounds__(NWAVES * 64, 2) mega_fwd(Args args) {
;     ...
;                     for (int half = 0; half < 2; ++half) { const f16x8 kf0 = kfr[ti][half][0], kf1 = kfr[ti][half][1];
;                         fa::f32x16 sc;
; #pragma unroll
;                         for (int r = 0; r < 16; ++r) sc[r] = 0.f;
;                         sc = __builtin_amdgcn_mfma_f32_32x32x16_f16(kf0, __builtin_bit_cast(f16x8, iqL[16 * 64 + lane]), sc, 0, 0, 0);
;                         sc = __builtin_amdgcn_mfma_f32_32x32x16_f16(kf1, __builtin_bit_cast(f16x8, iqL[17 * 64 + lane]), sc, 0, 0, 0);
; #pragma unroll 2
;                         for (int h = 0; h < 8; ++h) { fa::f32x16 a;
; #pragma unroll
;                             for (int r = 0; r < 16; ++r) a[r] = 0.f;
;                             a = __builtin_amdgcn_mfma_f32_32x32x16_f16(kf0, __builtin_bit_cast(f16x8, iqL[(2 * h) * 64 + lane]), a, 0, 0, 0);
;                             a = __builtin_amdgcn_mfma_f32_32x32x16_f16(kf1, __builtin_bit_cast(f16x8, iqL[(2 * h + 1) * 64 + lane]), a, 0, 0, 0);
;                             const float sg = ((sgnbits >> h) & 1u) ? -1.f : 1.f;
; #pragma unroll
;                             for (int r = 0; r < 16; ++r) sc[r] = __builtin_fmaf(__builtin_fabsf(a[r]), sg, sc[r]); }
; #pragma unroll
;                         for (int r = 0; r < 16; ++r) keys[ti][16 * half + r] = ordkey(sc[r]);
;                         if (k0 + 63 > 32 * qg) {
; #pragma unroll
;                             for (int r = 0; r < 16; ++r) { const int kidx = k0 + 32 * half + fa::crow(r, hi); keys[ti][16 * half + r] = (kidx <= t) ? keys[ti][16 * half + r] : 0u; } } }
.LBB0_624:
	v_mfma_f32_32x32x16_f16 v[2:17], v[82:85], v[106:109], 0
	s_mov_b32 s26, 0
	v_mov_b32_e32 v106, v141
	v_mfma_f32_32x32x16_f16 v[2:17], v[62:65], v[102:105], v[2:17]
	ds_read_b128 v[172:175], v106
	ds_read_b128 v[196:199], v106 offset:1024
	ds_read_b128 v[224:227], v106 offset:2048
	ds_read_b128 v[176:179], v106 offset:3072
.LBB0_625:
	s_waitcnt lgkmcnt(3)
	v_mfma_f32_32x32x16_f16 v[18:33], v[82:85], v[172:175], 0
	s_waitcnt lgkmcnt(2)
	v_mfma_f32_32x32x16_f16 v[18:33], v[62:65], v[196:199], v[18:33]
	s_waitcnt lgkmcnt(1)
	v_mfma_f32_32x32x16_f16 v[208:223], v[82:85], v[224:227], 0
	s_waitcnt lgkmcnt(0)
	v_mfma_f32_32x32x16_f16 v[208:223], v[62:65], v[176:179], v[208:223]
	v_add_u32_e32 v106, 0x1000, v106
	ds_read_b128 v[172:175], v106
	ds_read_b128 v[196:199], v106 offset:1024
	ds_read_b128 v[224:227], v106 offset:2048
	ds_read_b128 v[176:179], v106 offset:3072
	v_bfe_u32 v102, v140, s26, 1
	v_cmp_eq_u32_e32 vcc, 0, v102
	v_lshrrev_b32_e32 v180, s26, v140
	v_and_b32_e32 v180, 2, v180
	v_cndmask_b32_e64 v102, -1.0, 1.0, vcc
	v_cmp_eq_u32_e32 vcc, 0, v180
	s_add_i32 s26, s26, 2
	v_cndmask_b32_e64 v180, -1.0, 1.0, vcc
	s_cmp_lg_u32 s26, 8
	v_fma_f32 v104, |v18|, v102, v2
	v_fma_f32 v105, |v19|, v102, v3
	v_fma_f32 v108, |v20|, v102, v4
	v_fma_f32 v109, |v21|, v102, v5
	v_fma_f32 v22, |v22|, v102, v6
	v_fma_f32 v23, |v23|, v102, v7
	v_fma_f32 v24, |v24|, v102, v8
	v_fma_f32 v25, |v25|, v102, v9
	v_fma_f32 v26, |v26|, v102, v10
	v_fma_f32 v27, |v27|, v102, v11
	v_fma_f32 v28, |v28|, v102, v12
	v_fma_f32 v29, |v29|, v102, v13
	v_fma_f32 v30, |v30|, v102, v14
	v_fma_f32 v31, |v31|, v102, v15
	v_fma_f32 v32, |v32|, v102, v16
	v_fma_f32 v33, |v33|, v102, v17
	v_fma_f32 v4, |v210|, v180, v108
	v_fma_f32 v5, |v211|, v180, v109
	v_fma_f32 v2, |v208|, v180, v104
	v_fma_f32 v3, |v209|, v180, v105
	v_fma_f32 v8, |v214|, v180, v24
	v_fma_f32 v9, |v215|, v180, v25
	v_fma_f32 v6, |v212|, v180, v22
	v_fma_f32 v7, |v213|, v180, v23
	v_fma_f32 v12, |v218|, v180, v28
	v_fma_f32 v13, |v219|, v180, v29
	v_fma_f32 v10, |v216|, v180, v26
	v_fma_f32 v11, |v217|, v180, v27
	v_fma_f32 v16, |v222|, v180, v32
	v_fma_f32 v17, |v223|, v180, v33
	v_fma_f32 v14, |v220|, v180, v30
	v_fma_f32 v15, |v221|, v180, v31
	s_cbranch_scc1 .LBB0_625
	s_waitcnt lgkmcnt(0)
	v_ashrrev_i32_e32 v18, 31, v2
	v_ashrrev_i32_e32 v19, 31, v3
	v_ashrrev_i32_e32 v20, 31, v4
	v_ashrrev_i32_e32 v21, 31, v5
	v_bitop3_b32 v134, v21, v5, s68 bitop3:0x36
	v_bitop3_b32 v138, v20, v4, s68 bitop3:0x36
	v_bitop3_b32 v136, v19, v3, s68 bitop3:0x36
	v_bitop3_b32 v139, v18, v2, s68 bitop3:0x36
	v_ashrrev_i32_e32 v2, 31, v6
	v_ashrrev_i32_e32 v3, 31, v7
	v_ashrrev_i32_e32 v4, 31, v8
	v_ashrrev_i32_e32 v5, 31, v9
	v_bitop3_b32 v131, v5, v9, s68 bitop3:0x36
	v_bitop3_b32 v133, v4, v8, s68 bitop3:0x36
	v_bitop3_b32 v137, v3, v7, s68 bitop3:0x36
	v_bitop3_b32 v135, v2, v6, s68 bitop3:0x36
	v_ashrrev_i32_e32 v2, 31, v10
	v_ashrrev_i32_e32 v3, 31, v11
	v_ashrrev_i32_e32 v4, 31, v12
	v_ashrrev_i32_e32 v5, 31, v13
	v_bitop3_b32 v129, v5, v13, s68 bitop3:0x36
	v_bitop3_b32 v126, v4, v12, s68 bitop3:0x36
	v_bitop3_b32 v127, v3, v11, s68 bitop3:0x36
	v_bitop3_b32 v132, v2, v10, s68 bitop3:0x36
	v_ashrrev_i32_e32 v2, 31, v14
	v_ashrrev_i32_e32 v3, 31, v15
	v_ashrrev_i32_e32 v4, 31, v16
	v_ashrrev_i32_e32 v5, 31, v17
	v_bitop3_b32 v62, v5, v17, s68 bitop3:0x36
	v_bitop3_b32 v125, v4, v16, s68 bitop3:0x36
	v_bitop3_b32 v128, v3, v15, s68 bitop3:0x36
	s_andn2_b64 vcc, exec, s[40:41]
	v_bitop3_b32 v130, v2, v14, s68 bitop3:0x36
	s_cbranch_vccnz .LBB0_628
	v_add_u32_e32 v2, 32, v118
	v_or_b32_e32 v4, 2, v2
	v_or_b32_e32 v3, 3, v2
	v_cmp_le_i32_e32 vcc, v4, v124
	v_add_u32_e32 v5, 40, v118
	v_add_u32_e32 v4, 41, v118
	v_cndmask_b32_e32 v138, 0, v138, vcc
	v_cmp_le_i32_e32 vcc, v3, v124
	v_add_u32_e32 v3, 42, v118
	s_nop 0
	v_cndmask_b32_e32 v134, 0, v134, vcc
	v_cmp_le_i32_e32 vcc, v2, v124
	s_nop 1
	v_cndmask_b32_e32 v139, 0, v139, vcc
	v_cmp_gt_i32_e32 vcc, v124, v2
	v_add_u32_e32 v2, 43, v118
	s_nop 0
	v_cndmask_b32_e32 v136, 0, v136, vcc
	v_cmp_le_i32_e32 vcc, v5, v124
	v_add_u32_e32 v5, 48, v118
	s_nop 0
	v_cndmask_b32_e32 v135, 0, v135, vcc
	v_cmp_le_i32_e32 vcc, v4, v124
	v_add_u32_e32 v4, 49, v118
	s_nop 0
	v_cndmask_b32_e32 v137, 0, v137, vcc
	v_cmp_le_i32_e32 vcc, v3, v124
	v_add_u32_e32 v3, 50, v118
	s_nop 0
	v_cndmask_b32_e32 v133, 0, v133, vcc
	v_cmp_le_i32_e32 vcc, v2, v124
	v_add_u32_e32 v2, 51, v118
	s_nop 0
	v_cndmask_b32_e32 v131, 0, v131, vcc
	v_cmp_le_i32_e32 vcc, v5, v124
	v_add_u32_e32 v5, 56, v118
	s_nop 0
	v_cndmask_b32_e32 v132, 0, v132, vcc
	v_cmp_le_i32_e32 vcc, v4, v124
	v_add_u32_e32 v4, 57, v118
	s_nop 0
	v_cndmask_b32_e32 v127, 0, v127, vcc
	v_cmp_le_i32_e32 vcc, v3, v124
	v_add_u32_e32 v3, 58, v118
	s_nop 0
	v_cndmask_b32_e32 v126, 0, v126, vcc
	v_cmp_le_i32_e32 vcc, v2, v124
	v_add_u32_e32 v2, 59, v118
	s_nop 0
	v_cndmask_b32_e32 v129, 0, v129, vcc
	v_cmp_le_i32_e32 vcc, v5, v124
	s_nop 1
	v_cndmask_b32_e32 v130, 0, v130, vcc
	v_cmp_le_i32_e32 vcc, v4, v124
	s_nop 1
	v_cndmask_b32_e32 v128, 0, v128, vcc
	v_cmp_le_i32_e32 vcc, v3, v124
	s_nop 1
	v_cndmask_b32_e32 v125, 0, v125, vcc
	v_cmp_le_i32_e32 vcc, v2, v124
	s_nop 1
	v_cndmask_b32_e32 v62, 0, v62, vcc

; __device__ __forceinline__ unsigned ordkey(float f) { const unsigned u = __float_as_uint(f); return u ^ ((unsigned)((int)u >> 31) | 0x80000000u); }
; __device__ __forceinline__ int crow(int r, int hi) { return (r & 3) + 8 * (r >> 2) + 4 * hi; }
; __global__ void __launch_bounds__(NWAVES * 64, 2) mega_fwd(Args args) {
;     ...
;                     for (int half = 0; half < 2; ++half) { const f16x8 kf0 = kfr[ti][half][0], kf1 = kfr[ti][half][1];
;                         fa::f32x16 sc;
; #pragma unroll
;                         for (int r = 0; r < 16; ++r) sc[r] = 0.f;
;                         sc = __builtin_amdgcn_mfma_f32_32x32x16_f16(kf0, __builtin_bit_cast(f16x8, iqL[16 * 64 + lane]), sc, 0, 0, 0);
;                         sc = __builtin_amdgcn_mfma_f32_32x32x16_f16(kf1, __builtin_bit_cast(f16x8, iqL[17 * 64 + lane]), sc, 0, 0, 0);
; #pragma unroll 2
;                         for (int h = 0; h < 8; ++h) { fa::f32x16 a;
; #pragma unroll
;                             for (int r = 0; r < 16; ++r) a[r] = 0.f;
;                             a = __builtin_amdgcn_mfma_f32_32x32x16_f16(kf0, __builtin_bit_cast(f16x8, iqL[(2 * h) * 64 + lane]), a, 0, 0, 0);
;                             a = __builtin_amdgcn_mfma_f32_32x32x16_f16(kf1, __builtin_bit_cast(f16x8, iqL[(2 * h + 1) * 64 + lane]), a, 0, 0, 0);
;                             const float sg = ((sgnbits >> h) & 1u) ? -1.f : 1.f;
; #pragma unroll
;                             for (int r = 0; r < 16; ++r) sc[r] = __builtin_fmaf(__builtin_fabsf(a[r]), sg, sc[r]); }
; #pragma unroll
;                         for (int r = 0; r < 16; ++r) keys[ti][16 * half + r] = ordkey(sc[r]);
;                         if (k0 + 63 > 32 * qg) {
; #pragma unroll
;                             for (int r = 0; r < 16; ++r) { const int kidx = k0 + 32 * half + fa::crow(r, hi); keys[ti][16 * half + r] = (kidx <= t) ? keys[ti][16 * half + r] : 0u; } } }
.LBB0_629:
	ds_read_b128 v[106:109], v141 offset:16384
	ds_read_b128 v[102:105], v141 offset:17408
	v_mov_b32_e32 v63, v141
	s_waitcnt lgkmcnt(1)
	v_mfma_f32_32x32x16_f16 v[2:17], v[78:81], v[106:109], 0
	s_waitcnt lgkmcnt(0)
	v_mfma_f32_32x32x16_f16 v[2:17], v[74:77], v[102:105], v[2:17]
	s_nop 11
	v_mov_b32_e32 v65, v2
	v_mov_b32_e32 v2, v3
	v_mov_b32_e32 v64, v4
	v_mov_b32_e32 v3, v5
	ds_read_b128 v[172:175], v63
	ds_read_b128 v[196:199], v63 offset:1024
	ds_read_b128 v[224:227], v63 offset:2048
	ds_read_b128 v[176:179], v63 offset:3072
.LBB0_630:
	s_waitcnt lgkmcnt(3)
	v_mfma_f32_32x32x16_f16 v[18:33], v[78:81], v[172:175], 0
	s_waitcnt lgkmcnt(2)
	v_mfma_f32_32x32x16_f16 v[18:33], v[74:77], v[196:199], v[18:33]
	s_waitcnt lgkmcnt(1)
	v_mfma_f32_32x32x16_f16 v[208:223], v[78:81], v[224:227], 0
	s_waitcnt lgkmcnt(0)
	v_mfma_f32_32x32x16_f16 v[208:223], v[74:77], v[176:179], v[208:223]
	v_add_u32_e32 v63, 0x1000, v63
	ds_read_b128 v[172:175], v63
	ds_read_b128 v[196:199], v63 offset:1024
	ds_read_b128 v[224:227], v63 offset:2048
	ds_read_b128 v[176:179], v63 offset:3072
	v_bfe_u32 v4, v140, s26, 1
	v_cmp_eq_u32_e32 vcc, 0, v4
	v_lshrrev_b32_e32 v180, s26, v140
	v_and_b32_e32 v180, 2, v180
	v_cndmask_b32_e64 v4, -1.0, 1.0, vcc
	v_cmp_eq_u32_e32 vcc, 0, v180
	s_add_i32 s26, s26, 2
	v_cndmask_b32_e64 v180, -1.0, 1.0, vcc
	s_cmp_lg_u32 s26, 8
	v_fma_f32 v64, |v20|, v4, v64
	v_fma_f32 v65, |v18|, v4, v65
	v_fma_f32 v82, |v19|, v4, v2
	v_fma_f32 v83, |v21|, v4, v3
	v_fma_f32 v22, |v22|, v4, v6
	v_fma_f32 v23, |v23|, v4, v7
	v_fma_f32 v24, |v24|, v4, v8
	v_fma_f32 v25, |v25|, v4, v9
	v_fma_f32 v26, |v26|, v4, v10
	v_fma_f32 v27, |v27|, v4, v11
	v_fma_f32 v28, |v28|, v4, v12
	v_fma_f32 v29, |v29|, v4, v13
	v_fma_f32 v30, |v30|, v4, v14
	v_fma_f32 v31, |v31|, v4, v15
	v_fma_f32 v32, |v32|, v4, v16
	v_fma_f32 v33, |v33|, v4, v17
	v_fma_f32 v64, |v210|, v180, v64
	v_fma_f32 v65, |v208|, v180, v65
	v_fma_f32 v2, |v209|, v180, v82
	v_fma_f32 v3, |v211|, v180, v83
	v_fma_f32 v8, |v214|, v180, v24
	v_fma_f32 v9, |v215|, v180, v25
	v_fma_f32 v6, |v212|, v180, v22
	v_fma_f32 v7, |v213|, v180, v23
	v_fma_f32 v12, |v218|, v180, v28
	v_fma_f32 v13, |v219|, v180, v29
	v_fma_f32 v10, |v216|, v180, v26
	v_fma_f32 v11, |v217|, v180, v27
	v_fma_f32 v16, |v222|, v180, v32
	v_fma_f32 v17, |v223|, v180, v33
	v_fma_f32 v14, |v220|, v180, v30
	v_fma_f32 v15, |v221|, v180, v31
	s_cbranch_scc1 .LBB0_630
	s_waitcnt lgkmcnt(0)
	v_ashrrev_i32_e32 v4, 31, v65
	v_ashrrev_i32_e32 v5, 31, v64
	v_or_b32_e32 v4, 0x80000000, v4
	v_or_b32_e32 v5, 0x80000000, v5
	v_xor_b32_e32 v119, v4, v65
	v_xor_b32_e32 v118, v5, v64
	v_ashrrev_i32_e32 v4, 31, v3
	v_ashrrev_i32_e32 v5, 31, v2
	v_or_b32_e32 v4, 0x80000000, v4
	v_or_b32_e32 v5, 0x80000000, v5
	v_xor_b32_e32 v121, v4, v3
	v_xor_b32_e32 v120, v5, v2
	v_ashrrev_i32_e32 v2, 31, v6
	v_ashrrev_i32_e32 v3, 31, v7
	v_ashrrev_i32_e32 v4, 31, v8
	v_ashrrev_i32_e32 v5, 31, v9
	v_readlane_b32 s26, v254, 34
	v_bitop3_b32 v85, v5, v9, s68 bitop3:0x36
	v_bitop3_b32 v84, v4, v8, s68 bitop3:0x36
	v_bitop3_b32 v83, v3, v7, s68 bitop3:0x36
	v_bitop3_b32 v82, v2, v6, s68 bitop3:0x36
	v_ashrrev_i32_e32 v2, 31, v10
	v_ashrrev_i32_e32 v3, 31, v11
	v_ashrrev_i32_e32 v4, 31, v12
	v_ashrrev_i32_e32 v5, 31, v13
	s_cmp_gt_u32 s26, s44
	v_readlane_b32 s28, v253, 13
	v_bitop3_b32 v77, v5, v13, s68 bitop3:0x36
	v_bitop3_b32 v76, v4, v12, s68 bitop3:0x36
	v_bitop3_b32 v75, v3, v11, s68 bitop3:0x36
	v_bitop3_b32 v74, v2, v10, s68 bitop3:0x36
	v_ashrrev_i32_e32 v2, 31, v14
	v_ashrrev_i32_e32 v3, 31, v15
	v_ashrrev_i32_e32 v4, 31, v16
	v_ashrrev_i32_e32 v5, 31, v17
	s_cselect_b64 s[40:41], -1, 0
	s_cmp_le_u32 s26, s44
	v_add_u32_e32 v122, s28, v142
	v_bitop3_b32 v81, v5, v17, s68 bitop3:0x36
	v_bitop3_b32 v80, v4, v16, s68 bitop3:0x36
	v_bitop3_b32 v79, v3, v15, s68 bitop3:0x36
	v_bitop3_b32 v78, v2, v14, s68 bitop3:0x36
	v_readlane_b32 s29, v253, 14
	s_cbranch_scc1 .LBB0_633
	v_or_b32_e32 v2, 2, v122
	v_cmp_le_i32_e32 vcc, v122, v124
	v_add_u32_e32 v5, 11, v122
	v_add_u32_e32 v4, 10, v122
	v_cndmask_b32_e32 v119, 0, v119, vcc
	v_cmp_le_i32_e32 vcc, v2, v124
	v_or_b32_e32 v2, 3, v122
	v_add_u32_e32 v3, 9, v122
	v_cndmask_b32_e32 v118, 0, v118, vcc
	v_cmp_lt_i32_e32 vcc, v122, v124
	s_nop 1
	v_cndmask_b32_e32 v120, 0, v120, vcc
	v_cmp_ge_i32_e32 vcc, v124, v2
	v_add_u32_e32 v2, 8, v122
	s_nop 0
	v_cndmask_b32_e32 v121, 0, v121, vcc
	v_cmp_le_i32_e32 vcc, v5, v124
	v_add_u32_e32 v5, 19, v122
	s_nop 0
	v_cndmask_b32_e32 v85, 0, v85, vcc
	v_cmp_le_i32_e32 vcc, v4, v124
	v_add_u32_e32 v4, 18, v122
	s_nop 0
	v_cndmask_b32_e32 v84, 0, v84, vcc
	v_cmp_le_i32_e32 vcc, v3, v124
	v_add_u32_e32 v3, 17, v122
	s_nop 0
	v_cndmask_b32_e32 v83, 0, v83, vcc
	v_cmp_le_i32_e32 vcc, v2, v124
	v_add_u32_e32 v2, 16, v122
	s_nop 0
	v_cndmask_b32_e32 v82, 0, v82, vcc
	v_cmp_le_i32_e32 vcc, v5, v124
	v_add_u32_e32 v5, 27, v122
	s_nop 0
	v_cndmask_b32_e32 v77, 0, v77, vcc
	v_cmp_le_i32_e32 vcc, v4, v124
	v_add_u32_e32 v4, 26, v122
	s_nop 0
	v_cndmask_b32_e32 v76, 0, v76, vcc
	v_cmp_le_i32_e32 vcc, v3, v124
	v_add_u32_e32 v3, 25, v122
	s_nop 0
	v_cndmask_b32_e32 v75, 0, v75, vcc
	v_cmp_le_i32_e32 vcc, v2, v124
	v_add_u32_e32 v2, 24, v122
	s_nop 0
	v_cndmask_b32_e32 v74, 0, v74, vcc
	v_cmp_le_i32_e32 vcc, v5, v124
	s_nop 1
	v_cndmask_b32_e32 v81, 0, v81, vcc
	v_cmp_le_i32_e32 vcc, v4, v124
	s_nop 1
	v_cndmask_b32_e32 v80, 0, v80, vcc
	v_cmp_le_i32_e32 vcc, v3, v124
	s_nop 1
	v_cndmask_b32_e32 v79, 0, v79, vcc
	v_cmp_le_i32_e32 vcc, v2, v124
	s_nop 1
	v_cndmask_b32_e32 v78, 0, v78, vcc
; __device__ __forceinline__ unsigned ordkey(float f) { const unsigned u = __float_as_uint(f); return u ^ ((unsigned)((int)u >> 31) | 0x80000000u); }
; __device__ __forceinline__ int crow(int r, int hi) { return (r & 3) + 8 * (r >> 2) + 4 * hi; }
; __global__ void __launch_bounds__(NWAVES * 64, 2) mega_fwd(Args args) {
;     ...
;                     for (int half = 0; half < 2; ++half) { const f16x8 kf0 = kfr[ti][half][0], kf1 = kfr[ti][half][1];
;                         fa::f32x16 sc;
; #pragma unroll
;                         for (int r = 0; r < 16; ++r) sc[r] = 0.f;
;                         sc = __builtin_amdgcn_mfma_f32_32x32x16_f16(kf0, __builtin_bit_cast(f16x8, iqL[16 * 64 + lane]), sc, 0, 0, 0);
;                         sc = __builtin_amdgcn_mfma_f32_32x32x16_f16(kf1, __builtin_bit_cast(f16x8, iqL[17 * 64 + lane]), sc, 0, 0, 0);
; #pragma unroll 2
;                         for (int h = 0; h < 8; ++h) { fa::f32x16 a;
; #pragma unroll
;                             for (int r = 0; r < 16; ++r) a[r] = 0.f;
;                             a = __builtin_amdgcn_mfma_f32_32x32x16_f16(kf0, __builtin_bit_cast(f16x8, iqL[(2 * h) * 64 + lane]), a, 0, 0, 0);
;                             a = __builtin_amdgcn_mfma_f32_32x32x16_f16(kf1, __builtin_bit_cast(f16x8, iqL[(2 * h + 1) * 64 + lane]), a, 0, 0, 0);
;                             const float sg = ((sgnbits >> h) & 1u) ? -1.f : 1.f;
; #pragma unroll
;                             for (int r = 0; r < 16; ++r) sc[r] = __builtin_fmaf(__builtin_fabsf(a[r]), sg, sc[r]); }
; #pragma unroll
;                         for (int r = 0; r < 16; ++r) keys[ti][16 * half + r] = ordkey(sc[r]);
;                         if (k0 + 63 > 32 * qg) {
; #pragma unroll
;                             for (int r = 0; r < 16; ++r) { const int kidx = k0 + 32 * half + fa::crow(r, hi); keys[ti][16 * half + r] = (kidx <= t) ? keys[ti][16 * half + r] : 0u; } } }
.LBB0_633:
	v_mfma_f32_32x32x16_f16 v[2:17], v[98:101], v[106:109], 0
	s_mov_b32 s26, 0
	v_mov_b32_e32 v63, v141
	v_mfma_f32_32x32x16_f16 v[2:17], v[94:97], v[102:105], v[2:17]
	ds_read_b128 v[172:175], v63
	ds_read_b128 v[196:199], v63 offset:1024
	ds_read_b128 v[224:227], v63 offset:2048
	ds_read_b128 v[176:179], v63 offset:3072
.LBB0_634:
	s_waitcnt lgkmcnt(3)
	v_mfma_f32_32x32x16_f16 v[18:33], v[98:101], v[172:175], 0
	s_waitcnt lgkmcnt(2)
	v_mfma_f32_32x32x16_f16 v[18:33], v[94:97], v[196:199], v[18:33]
	s_waitcnt lgkmcnt(1)
	v_mfma_f32_32x32x16_f16 v[208:223], v[98:101], v[224:227], 0
	s_waitcnt lgkmcnt(0)
	v_mfma_f32_32x32x16_f16 v[208:223], v[94:97], v[176:179], v[208:223]
	v_add_u32_e32 v63, 0x1000, v63
	ds_read_b128 v[172:175], v63
	ds_read_b128 v[196:199], v63 offset:1024
	ds_read_b128 v[224:227], v63 offset:2048
	ds_read_b128 v[176:179], v63 offset:3072
	v_bfe_u32 v64, v140, s26, 1
	v_cmp_eq_u32_e32 vcc, 0, v64
	v_lshrrev_b32_e32 v180, s26, v140
	v_and_b32_e32 v180, 2, v180
	v_cndmask_b32_e64 v64, -1.0, 1.0, vcc
	v_cmp_eq_u32_e32 vcc, 0, v180
	s_add_i32 s26, s26, 2
	v_cndmask_b32_e64 v180, -1.0, 1.0, vcc
	s_cmp_lg_u32 s26, 8
	v_fma_f32 v102, |v18|, v64, v2
	v_fma_f32 v103, |v19|, v64, v3
	v_fma_f32 v104, |v20|, v64, v4
	v_fma_f32 v105, |v21|, v64, v5
	v_fma_f32 v22, |v22|, v64, v6
	v_fma_f32 v23, |v23|, v64, v7
	v_fma_f32 v24, |v24|, v64, v8
	v_fma_f32 v25, |v25|, v64, v9
	v_fma_f32 v26, |v26|, v64, v10
	v_fma_f32 v27, |v27|, v64, v11
	v_fma_f32 v28, |v28|, v64, v12
	v_fma_f32 v29, |v29|, v64, v13
	v_fma_f32 v30, |v30|, v64, v14
	v_fma_f32 v31, |v31|, v64, v15
	v_fma_f32 v32, |v32|, v64, v16
	v_fma_f32 v33, |v33|, v64, v17
	v_fma_f32 v4, |v210|, v180, v104
	v_fma_f32 v5, |v211|, v180, v105
	v_fma_f32 v2, |v208|, v180, v102
	v_fma_f32 v3, |v209|, v180, v103
	v_fma_f32 v8, |v214|, v180, v24
	v_fma_f32 v9, |v215|, v180, v25
	v_fma_f32 v6, |v212|, v180, v22
	v_fma_f32 v7, |v213|, v180, v23
	v_fma_f32 v12, |v218|, v180, v28
	v_fma_f32 v13, |v219|, v180, v29
	v_fma_f32 v10, |v216|, v180, v26
	v_fma_f32 v11, |v217|, v180, v27
	v_fma_f32 v16, |v222|, v180, v32
	v_fma_f32 v17, |v223|, v180, v33
	v_fma_f32 v14, |v220|, v180, v30
	v_fma_f32 v15, |v221|, v180, v31
	s_cbranch_scc1 .LBB0_634
	s_waitcnt lgkmcnt(0)
	v_ashrrev_i32_e32 v18, 31, v2
	v_ashrrev_i32_e32 v19, 31, v3
	v_ashrrev_i32_e32 v20, 31, v4
	v_ashrrev_i32_e32 v21, 31, v5
	v_bitop3_b32 v151, v21, v5, s68 bitop3:0x36
	v_bitop3_b32 v155, v20, v4, s68 bitop3:0x36
	v_bitop3_b32 v153, v19, v3, s68 bitop3:0x36
	v_bitop3_b32 v156, v18, v2, s68 bitop3:0x36
	v_ashrrev_i32_e32 v2, 31, v6
	v_ashrrev_i32_e32 v3, 31, v7
	v_ashrrev_i32_e32 v4, 31, v8
	v_ashrrev_i32_e32 v5, 31, v9
	v_bitop3_b32 v148, v5, v9, s68 bitop3:0x36
	v_bitop3_b32 v150, v4, v8, s68 bitop3:0x36
	v_bitop3_b32 v154, v3, v7, s68 bitop3:0x36
	v_bitop3_b32 v152, v2, v6, s68 bitop3:0x36
	v_ashrrev_i32_e32 v2, 31, v10
	v_ashrrev_i32_e32 v3, 31, v11
	v_ashrrev_i32_e32 v4, 31, v12
	v_ashrrev_i32_e32 v5, 31, v13
	v_bitop3_b32 v146, v5, v13, s68 bitop3:0x36
	v_bitop3_b32 v143, v4, v12, s68 bitop3:0x36
	v_bitop3_b32 v144, v3, v11, s68 bitop3:0x36
	v_bitop3_b32 v149, v2, v10, s68 bitop3:0x36
	v_ashrrev_i32_e32 v2, 31, v14
	v_ashrrev_i32_e32 v3, 31, v15
	v_ashrrev_i32_e32 v4, 31, v16
	v_ashrrev_i32_e32 v5, 31, v17
	v_bitop3_b32 v94, v5, v17, s68 bitop3:0x36
	v_bitop3_b32 v63, v4, v16, s68 bitop3:0x36
	v_bitop3_b32 v145, v3, v15, s68 bitop3:0x36
	s_andn2_b64 vcc, exec, s[40:41]
	v_bitop3_b32 v147, v2, v14, s68 bitop3:0x36
	s_cbranch_vccnz .LBB0_637
	v_add_u32_e32 v2, 32, v122
	v_or_b32_e32 v4, 2, v2
	v_or_b32_e32 v3, 3, v2
	v_cmp_le_i32_e32 vcc, v4, v124
	v_add_u32_e32 v5, 40, v122
	v_add_u32_e32 v4, 41, v122
	v_cndmask_b32_e32 v155, 0, v155, vcc
	v_cmp_le_i32_e32 vcc, v3, v124
	v_add_u32_e32 v3, 42, v122
	s_nop 0
	v_cndmask_b32_e32 v151, 0, v151, vcc
	v_cmp_le_i32_e32 vcc, v2, v124
	s_nop 1
	v_cndmask_b32_e32 v156, 0, v156, vcc
	v_cmp_gt_i32_e32 vcc, v124, v2
	v_add_u32_e32 v2, 43, v122
	s_nop 0
	v_cndmask_b32_e32 v153, 0, v153, vcc
	v_cmp_le_i32_e32 vcc, v5, v124
	v_add_u32_e32 v5, 48, v122
	s_nop 0
	v_cndmask_b32_e32 v152, 0, v152, vcc
	v_cmp_le_i32_e32 vcc, v4, v124
	v_add_u32_e32 v4, 49, v122
	s_nop 0
	v_cndmask_b32_e32 v154, 0, v154, vcc
	v_cmp_le_i32_e32 vcc, v3, v124
	v_add_u32_e32 v3, 50, v122
	s_nop 0
	v_cndmask_b32_e32 v150, 0, v150, vcc
	v_cmp_le_i32_e32 vcc, v2, v124
	v_add_u32_e32 v2, 51, v122
	s_nop 0
	v_cndmask_b32_e32 v148, 0, v148, vcc
	v_cmp_le_i32_e32 vcc, v5, v124
	v_add_u32_e32 v5, 56, v122
	s_nop 0
	v_cndmask_b32_e32 v149, 0, v149, vcc
	v_cmp_le_i32_e32 vcc, v4, v124
	v_add_u32_e32 v4, 57, v122
	s_nop 0
	v_cndmask_b32_e32 v144, 0, v144, vcc
	v_cmp_le_i32_e32 vcc, v3, v124
	v_add_u32_e32 v3, 58, v122
	s_nop 0
	v_cndmask_b32_e32 v143, 0, v143, vcc
	v_cmp_le_i32_e32 vcc, v2, v124
	v_add_u32_e32 v2, 59, v122
	s_nop 0
	v_cndmask_b32_e32 v146, 0, v146, vcc
	v_cmp_le_i32_e32 vcc, v5, v124
	s_nop 1
	v_cndmask_b32_e32 v147, 0, v147, vcc
	v_cmp_le_i32_e32 vcc, v4, v124
	s_nop 1
	v_cndmask_b32_e32 v145, 0, v145, vcc
	v_cmp_le_i32_e32 vcc, v3, v124
	s_nop 1
	v_cndmask_b32_e32 v63, 0, v63, vcc
	v_cmp_le_i32_e32 vcc, v2, v124
	s_nop 1
	v_cndmask_b32_e32 v94, 0, v94, vcc

; __device__ __forceinline__ unsigned ordkey(float f) { const unsigned u = __float_as_uint(f); return u ^ ((unsigned)((int)u >> 31) | 0x80000000u); }
; __device__ __forceinline__ int crow(int r, int hi) { return (r & 3) + 8 * (r >> 2) + 4 * hi; }
; __global__ void __launch_bounds__(NWAVES * 64, 2) mega_fwd(Args args) {
;     ...
;                     for (int half = 0; half < 2; ++half) { const f16x8 kf0 = kfr[ti][half][0], kf1 = kfr[ti][half][1];
;                         fa::f32x16 sc;
; #pragma unroll
;                         for (int r = 0; r < 16; ++r) sc[r] = 0.f;
;                         sc = __builtin_amdgcn_mfma_f32_32x32x16_f16(kf0, __builtin_bit_cast(f16x8, iqL[16 * 64 + lane]), sc, 0, 0, 0);
;                         sc = __builtin_amdgcn_mfma_f32_32x32x16_f16(kf1, __builtin_bit_cast(f16x8, iqL[17 * 64 + lane]), sc, 0, 0, 0);
; #pragma unroll 2
;                         for (int h = 0; h < 8; ++h) { fa::f32x16 a;
; #pragma unroll
;                             for (int r = 0; r < 16; ++r) a[r] = 0.f;
;                             a = __builtin_amdgcn_mfma_f32_32x32x16_f16(kf0, __builtin_bit_cast(f16x8, iqL[(2 * h) * 64 + lane]), a, 0, 0, 0);
;                             a = __builtin_amdgcn_mfma_f32_32x32x16_f16(kf1, __builtin_bit_cast(f16x8, iqL[(2 * h + 1) * 64 + lane]), a, 0, 0, 0);
;                             const float sg = ((sgnbits >> h) & 1u) ? -1.f : 1.f;
; #pragma unroll
;                             for (int r = 0; r < 16; ++r) sc[r] = __builtin_fmaf(__builtin_fabsf(a[r]), sg, sc[r]); }
; #pragma unroll
;                         for (int r = 0; r < 16; ++r) keys[ti][16 * half + r] = ordkey(sc[r]);
;                         if (k0 + 63 > 32 * qg) {
; #pragma unroll
;                             for (int r = 0; r < 16; ++r) { const int kidx = k0 + 32 * half + fa::crow(r, hi); keys[ti][16 * half + r] = (kidx <= t) ? keys[ti][16 * half + r] : 0u; } } }
.LBB0_638:
	ds_read_b128 v[104:107], v141 offset:16384
	ds_read_b128 v[100:103], v141 offset:17408
	v_mov_b32_e32 v95, v141
	s_waitcnt lgkmcnt(1)
	v_mfma_f32_32x32x16_f16 v[2:17], v[90:93], v[104:107], 0
	s_waitcnt lgkmcnt(0)
	v_mfma_f32_32x32x16_f16 v[2:17], v[86:89], v[100:103], v[2:17]
	s_nop 11
	v_mov_b32_e32 v65, v2
	v_mov_b32_e32 v2, v3
	v_mov_b32_e32 v64, v4
	v_mov_b32_e32 v3, v5
	ds_read_b128 v[172:175], v95
	ds_read_b128 v[196:199], v95 offset:1024
	ds_read_b128 v[224:227], v95 offset:2048
	ds_read_b128 v[176:179], v95 offset:3072
.LBB0_639:
	s_waitcnt lgkmcnt(3)
	v_mfma_f32_32x32x16_f16 v[18:33], v[90:93], v[172:175], 0
	s_waitcnt lgkmcnt(2)
	v_mfma_f32_32x32x16_f16 v[18:33], v[86:89], v[196:199], v[18:33]
	s_waitcnt lgkmcnt(1)
	v_mfma_f32_32x32x16_f16 v[208:223], v[90:93], v[224:227], 0
	s_waitcnt lgkmcnt(0)
	v_mfma_f32_32x32x16_f16 v[208:223], v[86:89], v[176:179], v[208:223]
	v_add_u32_e32 v95, 0x1000, v95
	ds_read_b128 v[172:175], v95
	ds_read_b128 v[196:199], v95 offset:1024
	ds_read_b128 v[224:227], v95 offset:2048
	ds_read_b128 v[176:179], v95 offset:3072
	v_bfe_u32 v4, v140, s26, 1
	v_cmp_eq_u32_e32 vcc, 0, v4
	v_lshrrev_b32_e32 v180, s26, v140
	v_and_b32_e32 v180, 2, v180
	v_cndmask_b32_e64 v4, -1.0, 1.0, vcc
	v_cmp_eq_u32_e32 vcc, 0, v180
	s_add_i32 s26, s26, 2
	v_cndmask_b32_e64 v180, -1.0, 1.0, vcc
	s_cmp_lg_u32 s26, 8
	v_fma_f32 v64, |v20|, v4, v64
	v_fma_f32 v65, |v18|, v4, v65
	v_fma_f32 v96, |v19|, v4, v2
	v_fma_f32 v97, |v21|, v4, v3
	v_fma_f32 v22, |v22|, v4, v6
	v_fma_f32 v23, |v23|, v4, v7
	v_fma_f32 v24, |v24|, v4, v8
	v_fma_f32 v25, |v25|, v4, v9
	v_fma_f32 v26, |v26|, v4, v10
	v_fma_f32 v27, |v27|, v4, v11
	v_fma_f32 v28, |v28|, v4, v12
	v_fma_f32 v29, |v29|, v4, v13
	v_fma_f32 v30, |v30|, v4, v14
	v_fma_f32 v31, |v31|, v4, v15
	v_fma_f32 v32, |v32|, v4, v16
	v_fma_f32 v33, |v33|, v4, v17
	v_fma_f32 v64, |v210|, v180, v64
	v_fma_f32 v65, |v208|, v180, v65
	v_fma_f32 v2, |v209|, v180, v96
	v_fma_f32 v3, |v211|, v180, v97
	v_fma_f32 v8, |v214|, v180, v24
	v_fma_f32 v9, |v215|, v180, v25
	v_fma_f32 v6, |v212|, v180, v22
	v_fma_f32 v7, |v213|, v180, v23
	v_fma_f32 v12, |v218|, v180, v28
	v_fma_f32 v13, |v219|, v180, v29
	v_fma_f32 v10, |v216|, v180, v26
	v_fma_f32 v11, |v217|, v180, v27
	v_fma_f32 v16, |v222|, v180, v32
	v_fma_f32 v17, |v223|, v180, v33
	v_fma_f32 v14, |v220|, v180, v30
	v_fma_f32 v15, |v221|, v180, v31
	s_cbranch_scc1 .LBB0_639
	s_waitcnt lgkmcnt(0)
	v_ashrrev_i32_e32 v4, 31, v65
	v_ashrrev_i32_e32 v5, 31, v64
	v_or_b32_e32 v4, 0x80000000, v4
	v_or_b32_e32 v5, 0x80000000, v5
	v_xor_b32_e32 v109, v4, v65
	v_xor_b32_e32 v108, v5, v64
	v_ashrrev_i32_e32 v4, 31, v3
	v_ashrrev_i32_e32 v5, 31, v2
	v_or_b32_e32 v4, 0x80000000, v4
	v_or_b32_e32 v5, 0x80000000, v5
	v_xor_b32_e32 v123, v4, v3
	v_xor_b32_e32 v122, v5, v2
	v_ashrrev_i32_e32 v2, 31, v6
	v_ashrrev_i32_e32 v3, 31, v7
	v_ashrrev_i32_e32 v4, 31, v8
	v_ashrrev_i32_e32 v5, 31, v9
	v_readlane_b32 s26, v254, 35
	v_bitop3_b32 v99, v5, v9, s68 bitop3:0x36
	v_bitop3_b32 v98, v4, v8, s68 bitop3:0x36
	v_bitop3_b32 v97, v3, v7, s68 bitop3:0x36
	v_bitop3_b32 v96, v2, v6, s68 bitop3:0x36
	v_ashrrev_i32_e32 v2, 31, v10
	v_ashrrev_i32_e32 v3, 31, v11
	v_ashrrev_i32_e32 v4, 31, v12
	v_ashrrev_i32_e32 v5, 31, v13
	s_cmp_gt_u32 s26, s44
	v_readlane_b32 s28, v253, 39
	v_bitop3_b32 v89, v5, v13, s68 bitop3:0x36
	v_bitop3_b32 v88, v4, v12, s68 bitop3:0x36
	v_bitop3_b32 v87, v3, v11, s68 bitop3:0x36
	v_bitop3_b32 v86, v2, v10, s68 bitop3:0x36
	v_ashrrev_i32_e32 v2, 31, v14
	v_ashrrev_i32_e32 v3, 31, v15
	v_ashrrev_i32_e32 v4, 31, v16
	v_ashrrev_i32_e32 v5, 31, v17
	s_cselect_b64 s[40:41], -1, 0
	s_cmp_le_u32 s26, s44
	v_add_u32_e32 v171, s28, v142
	v_bitop3_b32 v93, v5, v17, s68 bitop3:0x36
	v_bitop3_b32 v92, v4, v16, s68 bitop3:0x36
	v_bitop3_b32 v91, v3, v15, s68 bitop3:0x36
	v_bitop3_b32 v90, v2, v14, s68 bitop3:0x36
	v_readlane_b32 s29, v253, 40
	s_cbranch_scc1 .LBB0_642
	v_or_b32_e32 v2, 2, v171
	v_cmp_le_i32_e32 vcc, v171, v124
	v_add_u32_e32 v5, 11, v171
	v_add_u32_e32 v4, 10, v171
	v_cndmask_b32_e32 v109, 0, v109, vcc
	v_cmp_le_i32_e32 vcc, v2, v124
	v_or_b32_e32 v2, 3, v171
	v_add_u32_e32 v3, 9, v171
	v_cndmask_b32_e32 v108, 0, v108, vcc
	v_cmp_lt_i32_e32 vcc, v171, v124
	s_nop 1
	v_cndmask_b32_e32 v122, 0, v122, vcc
	v_cmp_ge_i32_e32 vcc, v124, v2
	v_add_u32_e32 v2, 8, v171
	s_nop 0
	v_cndmask_b32_e32 v123, 0, v123, vcc
	v_cmp_le_i32_e32 vcc, v5, v124
	v_add_u32_e32 v5, 19, v171
	s_nop 0
	v_cndmask_b32_e32 v99, 0, v99, vcc
	v_cmp_le_i32_e32 vcc, v4, v124
	v_add_u32_e32 v4, 18, v171
	s_nop 0
	v_cndmask_b32_e32 v98, 0, v98, vcc
	v_cmp_le_i32_e32 vcc, v3, v124
	v_add_u32_e32 v3, 17, v171
	s_nop 0
	v_cndmask_b32_e32 v97, 0, v97, vcc
	v_cmp_le_i32_e32 vcc, v2, v124
	v_add_u32_e32 v2, 16, v171
	s_nop 0
	v_cndmask_b32_e32 v96, 0, v96, vcc
	v_cmp_le_i32_e32 vcc, v5, v124
	v_add_u32_e32 v5, 27, v171
	s_nop 0
	v_cndmask_b32_e32 v89, 0, v89, vcc
	v_cmp_le_i32_e32 vcc, v4, v124
	v_add_u32_e32 v4, 26, v171
	s_nop 0
	v_cndmask_b32_e32 v88, 0, v88, vcc
	v_cmp_le_i32_e32 vcc, v3, v124
	v_add_u32_e32 v3, 25, v171
	s_nop 0
	v_cndmask_b32_e32 v87, 0, v87, vcc
	v_cmp_le_i32_e32 vcc, v2, v124
	v_add_u32_e32 v2, 24, v171
	s_nop 0
	v_cndmask_b32_e32 v86, 0, v86, vcc
	v_cmp_le_i32_e32 vcc, v5, v124
	s_nop 1
	v_cndmask_b32_e32 v93, 0, v93, vcc
	v_cmp_le_i32_e32 vcc, v4, v124
	s_nop 1
	v_cndmask_b32_e32 v92, 0, v92, vcc
	v_cmp_le_i32_e32 vcc, v3, v124
	s_nop 1
	v_cndmask_b32_e32 v91, 0, v91, vcc
	v_cmp_le_i32_e32 vcc, v2, v124
	s_nop 1
	v_cndmask_b32_e32 v90, 0, v90, vcc
; __device__ __forceinline__ unsigned ordkey(float f) { const unsigned u = __float_as_uint(f); return u ^ ((unsigned)((int)u >> 31) | 0x80000000u); }
; __device__ __forceinline__ int crow(int r, int hi) { return (r & 3) + 8 * (r >> 2) + 4 * hi; }
; __global__ void __launch_bounds__(NWAVES * 64, 2) mega_fwd(Args args) {
;     ...
;                     for (int half = 0; half < 2; ++half) { const f16x8 kf0 = kfr[ti][half][0], kf1 = kfr[ti][half][1];
;                         fa::f32x16 sc;
; #pragma unroll
;                         for (int r = 0; r < 16; ++r) sc[r] = 0.f;
;                         sc = __builtin_amdgcn_mfma_f32_32x32x16_f16(kf0, __builtin_bit_cast(f16x8, iqL[16 * 64 + lane]), sc, 0, 0, 0);
;                         sc = __builtin_amdgcn_mfma_f32_32x32x16_f16(kf1, __builtin_bit_cast(f16x8, iqL[17 * 64 + lane]), sc, 0, 0, 0);
; #pragma unroll 2
;                         for (int h = 0; h < 8; ++h) { fa::f32x16 a;
; #pragma unroll
;                             for (int r = 0; r < 16; ++r) a[r] = 0.f;
;                             a = __builtin_amdgcn_mfma_f32_32x32x16_f16(kf0, __builtin_bit_cast(f16x8, iqL[(2 * h) * 64 + lane]), a, 0, 0, 0);
;                             a = __builtin_amdgcn_mfma_f32_32x32x16_f16(kf1, __builtin_bit_cast(f16x8, iqL[(2 * h + 1) * 64 + lane]), a, 0, 0, 0);
;                             const float sg = ((sgnbits >> h) & 1u) ? -1.f : 1.f;
; #pragma unroll
;                             for (int r = 0; r < 16; ++r) sc[r] = __builtin_fmaf(__builtin_fabsf(a[r]), sg, sc[r]); }
; #pragma unroll
;                         for (int r = 0; r < 16; ++r) keys[ti][16 * half + r] = ordkey(sc[r]);
;                         if (k0 + 63 > 32 * qg) {
; #pragma unroll
;                             for (int r = 0; r < 16; ++r) { const int kidx = k0 + 32 * half + fa::crow(r, hi); keys[ti][16 * half + r] = (kidx <= t) ? keys[ti][16 * half + r] : 0u; } } }
.LBB0_642:
	v_mfma_f32_32x32x16_f16 v[2:17], v[70:73], v[104:107], 0
	s_mov_b32 s26, 0
	v_mov_b32_e32 v64, v141
	v_mfma_f32_32x32x16_f16 v[2:17], v[66:69], v[100:103], v[2:17]
	ds_read_b128 v[172:175], v64
	ds_read_b128 v[196:199], v64 offset:1024
	ds_read_b128 v[224:227], v64 offset:2048
	ds_read_b128 v[176:179], v64 offset:3072
.LBB0_643:
	s_waitcnt lgkmcnt(3)
	v_mfma_f32_32x32x16_f16 v[18:33], v[70:73], v[172:175], 0
	s_waitcnt lgkmcnt(2)
	v_mfma_f32_32x32x16_f16 v[18:33], v[66:69], v[196:199], v[18:33]
	s_waitcnt lgkmcnt(1)
	v_mfma_f32_32x32x16_f16 v[208:223], v[70:73], v[224:227], 0
	s_waitcnt lgkmcnt(0)
	v_mfma_f32_32x32x16_f16 v[208:223], v[66:69], v[176:179], v[208:223]
	v_add_u32_e32 v64, 0x1000, v64
	ds_read_b128 v[172:175], v64
	ds_read_b128 v[196:199], v64 offset:1024
	ds_read_b128 v[224:227], v64 offset:2048
	ds_read_b128 v[176:179], v64 offset:3072
	v_bfe_u32 v100, v140, s26, 1
	v_cmp_eq_u32_e32 vcc, 0, v100
	v_lshrrev_b32_e32 v180, s26, v140
	v_and_b32_e32 v180, 2, v180
	v_cndmask_b32_e64 v100, -1.0, 1.0, vcc
	v_cmp_eq_u32_e32 vcc, 0, v180
	s_add_i32 s26, s26, 2
	v_cndmask_b32_e64 v180, -1.0, 1.0, vcc
	s_cmp_lg_u32 s26, 8
	v_fma_f32 v102, |v18|, v100, v2
	v_fma_f32 v103, |v19|, v100, v3
	v_fma_f32 v104, |v20|, v100, v4
	v_fma_f32 v105, |v21|, v100, v5
	v_fma_f32 v22, |v22|, v100, v6
	v_fma_f32 v23, |v23|, v100, v7
	v_fma_f32 v24, |v24|, v100, v8
	v_fma_f32 v25, |v25|, v100, v9
	v_fma_f32 v26, |v26|, v100, v10
	v_fma_f32 v27, |v27|, v100, v11
	v_fma_f32 v28, |v28|, v100, v12
	v_fma_f32 v29, |v29|, v100, v13
	v_fma_f32 v30, |v30|, v100, v14
	v_fma_f32 v31, |v31|, v100, v15
	v_fma_f32 v32, |v32|, v100, v16
	v_fma_f32 v33, |v33|, v100, v17
	v_fma_f32 v4, |v210|, v180, v104
	v_fma_f32 v5, |v211|, v180, v105
	v_fma_f32 v2, |v208|, v180, v102
	v_fma_f32 v3, |v209|, v180, v103
	v_fma_f32 v8, |v214|, v180, v24
	v_fma_f32 v9, |v215|, v180, v25
	v_fma_f32 v6, |v212|, v180, v22
	v_fma_f32 v7, |v213|, v180, v23
	v_fma_f32 v12, |v218|, v180, v28
	v_fma_f32 v13, |v219|, v180, v29
	v_fma_f32 v10, |v216|, v180, v26
	v_fma_f32 v11, |v217|, v180, v27
	v_fma_f32 v16, |v222|, v180, v32
	v_fma_f32 v17, |v223|, v180, v33
	v_fma_f32 v14, |v220|, v180, v30
	v_fma_f32 v15, |v221|, v180, v31
	s_cbranch_scc1 .LBB0_643
	s_waitcnt lgkmcnt(0)
	v_ashrrev_i32_e32 v18, 31, v2
	v_ashrrev_i32_e32 v19, 31, v3
	v_ashrrev_i32_e32 v20, 31, v4
	v_ashrrev_i32_e32 v21, 31, v5
	v_bitop3_b32 v165, v21, v5, s68 bitop3:0x36
	v_bitop3_b32 v169, v20, v4, s68 bitop3:0x36
	v_bitop3_b32 v167, v19, v3, s68 bitop3:0x36
	v_bitop3_b32 v170, v18, v2, s68 bitop3:0x36
	v_ashrrev_i32_e32 v2, 31, v6
	v_ashrrev_i32_e32 v3, 31, v7
	v_ashrrev_i32_e32 v4, 31, v8
	v_ashrrev_i32_e32 v5, 31, v9
	v_bitop3_b32 v162, v5, v9, s68 bitop3:0x36
	v_bitop3_b32 v164, v4, v8, s68 bitop3:0x36
	v_bitop3_b32 v168, v3, v7, s68 bitop3:0x36
	v_bitop3_b32 v166, v2, v6, s68 bitop3:0x36
	v_ashrrev_i32_e32 v2, 31, v10
	v_ashrrev_i32_e32 v3, 31, v11
	v_ashrrev_i32_e32 v4, 31, v12
	v_ashrrev_i32_e32 v5, 31, v13
	v_bitop3_b32 v160, v5, v13, s68 bitop3:0x36
	v_bitop3_b32 v157, v4, v12, s68 bitop3:0x36
	v_bitop3_b32 v158, v3, v11, s68 bitop3:0x36
	v_bitop3_b32 v163, v2, v10, s68 bitop3:0x36
	v_ashrrev_i32_e32 v2, 31, v14
	v_ashrrev_i32_e32 v3, 31, v15
	v_ashrrev_i32_e32 v4, 31, v16
	v_ashrrev_i32_e32 v5, 31, v17
	v_bitop3_b32 v64, v5, v17, s68 bitop3:0x36
	v_bitop3_b32 v95, v4, v16, s68 bitop3:0x36
	v_bitop3_b32 v159, v3, v15, s68 bitop3:0x36
	s_andn2_b64 vcc, exec, s[40:41]
	v_bitop3_b32 v161, v2, v14, s68 bitop3:0x36
	s_cbranch_vccnz .LBB0_646
	v_add_u32_e32 v2, 32, v171
	v_or_b32_e32 v4, 2, v2
	v_or_b32_e32 v3, 3, v2
	v_cmp_le_i32_e32 vcc, v4, v124
	v_add_u32_e32 v5, 40, v171
	v_add_u32_e32 v4, 41, v171
	v_cndmask_b32_e32 v169, 0, v169, vcc
	v_cmp_le_i32_e32 vcc, v3, v124
	v_add_u32_e32 v3, 42, v171
	s_nop 0
	v_cndmask_b32_e32 v165, 0, v165, vcc
	v_cmp_le_i32_e32 vcc, v2, v124
	s_nop 1
	v_cndmask_b32_e32 v170, 0, v170, vcc
	v_cmp_gt_i32_e32 vcc, v124, v2
	v_add_u32_e32 v2, 43, v171
	s_nop 0
	v_cndmask_b32_e32 v167, 0, v167, vcc
	v_cmp_le_i32_e32 vcc, v5, v124
	v_add_u32_e32 v5, 48, v171
	s_nop 0
	v_cndmask_b32_e32 v166, 0, v166, vcc
	v_cmp_le_i32_e32 vcc, v4, v124
	v_add_u32_e32 v4, 49, v171
	s_nop 0
	v_cndmask_b32_e32 v168, 0, v168, vcc
	v_cmp_le_i32_e32 vcc, v3, v124
	v_add_u32_e32 v3, 50, v171
	s_nop 0
	v_cndmask_b32_e32 v164, 0, v164, vcc
	v_cmp_le_i32_e32 vcc, v2, v124
	v_add_u32_e32 v2, 51, v171
	s_nop 0
	v_cndmask_b32_e32 v162, 0, v162, vcc
	v_cmp_le_i32_e32 vcc, v5, v124
	v_add_u32_e32 v5, 56, v171
	s_nop 0
	v_cndmask_b32_e32 v163, 0, v163, vcc
	v_cmp_le_i32_e32 vcc, v4, v124
	v_add_u32_e32 v4, 57, v171
	s_nop 0
	v_cndmask_b32_e32 v158, 0, v158, vcc
	v_cmp_le_i32_e32 vcc, v3, v124
	v_add_u32_e32 v3, 58, v171
	s_nop 0
	v_cndmask_b32_e32 v157, 0, v157, vcc
	v_cmp_le_i32_e32 vcc, v2, v124
	v_add_u32_e32 v2, 59, v171
	s_nop 0
	v_cndmask_b32_e32 v160, 0, v160, vcc
	v_cmp_le_i32_e32 vcc, v5, v124
	s_nop 1
	v_cndmask_b32_e32 v161, 0, v161, vcc
	v_cmp_le_i32_e32 vcc, v4, v124
	s_nop 1
	v_cndmask_b32_e32 v159, 0, v159, vcc
	v_cmp_le_i32_e32 vcc, v3, v124
	s_nop 1
	v_cndmask_b32_e32 v95, 0, v95, vcc
	v_cmp_le_i32_e32 vcc, v2, v124
	s_nop 1
	v_cndmask_b32_e32 v64, 0, v64, vcc

; __device__ __forceinline__ unsigned ordkey(float f) { const unsigned u = __float_as_uint(f); return u ^ ((unsigned)((int)u >> 31) | 0x80000000u); }
; __device__ __forceinline__ int crow(int r, int hi) { return (r & 3) + 8 * (r >> 2) + 4 * hi; }
; __global__ void __launch_bounds__(NWAVES * 64, 2) mega_fwd(Args args) {
;     ...
;                     for (int half = 0; half < 2; ++half) { const f16x8 kf0 = kfr[ti][half][0], kf1 = kfr[ti][half][1];
;                         fa::f32x16 sc;
; #pragma unroll
;                         for (int r = 0; r < 16; ++r) sc[r] = 0.f;
;                         sc = __builtin_amdgcn_mfma_f32_32x32x16_f16(kf0, __builtin_bit_cast(f16x8, iqL[16 * 64 + lane]), sc, 0, 0, 0);
;                         sc = __builtin_amdgcn_mfma_f32_32x32x16_f16(kf1, __builtin_bit_cast(f16x8, iqL[17 * 64 + lane]), sc, 0, 0, 0);
; #pragma unroll 2
;                         for (int h = 0; h < 8; ++h) { fa::f32x16 a;
; #pragma unroll
;                             for (int r = 0; r < 16; ++r) a[r] = 0.f;
;                             a = __builtin_amdgcn_mfma_f32_32x32x16_f16(kf0, __builtin_bit_cast(f16x8, iqL[(2 * h) * 64 + lane]), a, 0, 0, 0);
;                             a = __builtin_amdgcn_mfma_f32_32x32x16_f16(kf1, __builtin_bit_cast(f16x8, iqL[(2 * h + 1) * 64 + lane]), a, 0, 0, 0);
;                             const float sg = ((sgnbits >> h) & 1u) ? -1.f : 1.f;
; #pragma unroll
;                             for (int r = 0; r < 16; ++r) sc[r] = __builtin_fmaf(__builtin_fabsf(a[r]), sg, sc[r]); }
; #pragma unroll
;                         for (int r = 0; r < 16; ++r) keys[ti][16 * half + r] = ordkey(sc[r]);
;                         if (k0 + 63 > 32 * qg) {
; #pragma unroll
;                             for (int r = 0; r < 16; ++r) { const int kidx = k0 + 32 * half + fa::crow(r, hi); keys[ti][16 * half + r] = (kidx <= t) ? keys[ti][16 * half + r] : 0u; } } }
.LBB0_647:
	ds_read_b128 v[100:103], v141 offset:16384
	ds_read_b128 v[70:73], v141 offset:17408
	v_mov_b32_e32 v65, v141
	s_waitcnt lgkmcnt(1)
	v_mfma_f32_32x32x16_f16 v[2:17], v[58:61], v[100:103], 0
	s_waitcnt lgkmcnt(0)
	v_mfma_f32_32x32x16_f16 v[2:17], v[54:57], v[70:73], v[2:17]
	s_nop 11
	v_mov_b32_e32 v67, v2
	v_mov_b32_e32 v2, v3
	v_mov_b32_e32 v66, v4
	v_mov_b32_e32 v3, v5
	ds_read_b128 v[172:175], v65
	ds_read_b128 v[196:199], v65 offset:1024
	ds_read_b128 v[224:227], v65 offset:2048
	ds_read_b128 v[176:179], v65 offset:3072
.LBB0_648:
	s_waitcnt lgkmcnt(3)
	v_mfma_f32_32x32x16_f16 v[18:33], v[58:61], v[172:175], 0
	s_waitcnt lgkmcnt(2)
	v_mfma_f32_32x32x16_f16 v[18:33], v[54:57], v[196:199], v[18:33]
	s_waitcnt lgkmcnt(1)
	v_mfma_f32_32x32x16_f16 v[208:223], v[58:61], v[224:227], 0
	s_waitcnt lgkmcnt(0)
	v_mfma_f32_32x32x16_f16 v[208:223], v[54:57], v[176:179], v[208:223]
	v_add_u32_e32 v65, 0x1000, v65
	ds_read_b128 v[172:175], v65
	ds_read_b128 v[196:199], v65 offset:1024
	ds_read_b128 v[224:227], v65 offset:2048
	ds_read_b128 v[176:179], v65 offset:3072
	v_bfe_u32 v4, v140, s26, 1
	v_cmp_eq_u32_e32 vcc, 0, v4
	v_lshrrev_b32_e32 v180, s26, v140
	v_and_b32_e32 v180, 2, v180
	v_cndmask_b32_e64 v4, -1.0, 1.0, vcc
	v_cmp_eq_u32_e32 vcc, 0, v180
	s_add_i32 s26, s26, 2
	v_cndmask_b32_e64 v180, -1.0, 1.0, vcc
	s_cmp_lg_u32 s26, 8
	v_fma_f32 v66, |v20|, v4, v66
	v_fma_f32 v67, |v18|, v4, v67
	v_fma_f32 v68, |v19|, v4, v2
	v_fma_f32 v69, |v21|, v4, v3
	v_fma_f32 v22, |v22|, v4, v6
	v_fma_f32 v23, |v23|, v4, v7
	v_fma_f32 v24, |v24|, v4, v8
	v_fma_f32 v25, |v25|, v4, v9
	v_fma_f32 v26, |v26|, v4, v10
	v_fma_f32 v27, |v27|, v4, v11
	v_fma_f32 v28, |v28|, v4, v12
	v_fma_f32 v29, |v29|, v4, v13
	v_fma_f32 v30, |v30|, v4, v14
	v_fma_f32 v31, |v31|, v4, v15
	v_fma_f32 v32, |v32|, v4, v16
	v_fma_f32 v33, |v33|, v4, v17
	v_fma_f32 v66, |v210|, v180, v66
	v_fma_f32 v67, |v208|, v180, v67
	v_fma_f32 v2, |v209|, v180, v68
	v_fma_f32 v3, |v211|, v180, v69
	v_fma_f32 v8, |v214|, v180, v24
	v_fma_f32 v9, |v215|, v180, v25
	v_fma_f32 v6, |v212|, v180, v22
	v_fma_f32 v7, |v213|, v180, v23
	v_fma_f32 v12, |v218|, v180, v28
	v_fma_f32 v13, |v219|, v180, v29
	v_fma_f32 v10, |v216|, v180, v26
	v_fma_f32 v11, |v217|, v180, v27
	v_fma_f32 v16, |v222|, v180, v32
	v_fma_f32 v17, |v223|, v180, v33
	v_fma_f32 v14, |v220|, v180, v30
	v_fma_f32 v15, |v221|, v180, v31
	s_cbranch_scc1 .LBB0_648
	s_waitcnt lgkmcnt(0)
	v_ashrrev_i32_e32 v4, 31, v67
	v_ashrrev_i32_e32 v5, 31, v66
	v_or_b32_e32 v4, 0x80000000, v4
	v_or_b32_e32 v5, 0x80000000, v5
	v_xor_b32_e32 v105, v4, v67
	v_xor_b32_e32 v104, v5, v66
	v_ashrrev_i32_e32 v4, 31, v3
	v_ashrrev_i32_e32 v5, 31, v2
	v_or_b32_e32 v4, 0x80000000, v4
	v_or_b32_e32 v5, 0x80000000, v5
	v_xor_b32_e32 v107, v4, v3
	v_xor_b32_e32 v106, v5, v2
	v_ashrrev_i32_e32 v2, 31, v6
	v_ashrrev_i32_e32 v3, 31, v7
	v_ashrrev_i32_e32 v4, 31, v8
	v_ashrrev_i32_e32 v5, 31, v9
	v_readlane_b32 s26, v254, 36
	v_bitop3_b32 v69, v5, v9, s68 bitop3:0x36
	v_bitop3_b32 v68, v4, v8, s68 bitop3:0x36
	v_bitop3_b32 v67, v3, v7, s68 bitop3:0x36
	v_bitop3_b32 v66, v2, v6, s68 bitop3:0x36
	v_ashrrev_i32_e32 v2, 31, v10
	v_ashrrev_i32_e32 v3, 31, v11
	v_ashrrev_i32_e32 v4, 31, v12
	v_ashrrev_i32_e32 v5, 31, v13
	s_cmp_gt_u32 s26, s44
	v_readlane_b32 s28, v253, 4
	v_bitop3_b32 v57, v5, v13, s68 bitop3:0x36
	v_bitop3_b32 v56, v4, v12, s68 bitop3:0x36
	v_bitop3_b32 v55, v3, v11, s68 bitop3:0x36
	v_bitop3_b32 v54, v2, v10, s68 bitop3:0x36
	v_ashrrev_i32_e32 v2, 31, v14
	v_ashrrev_i32_e32 v3, 31, v15
	v_ashrrev_i32_e32 v4, 31, v16
	v_ashrrev_i32_e32 v5, 31, v17
	s_cselect_b64 s[40:41], -1, 0
	s_cmp_le_u32 s26, s44
	v_add_u32_e32 v65, s28, v142
	v_bitop3_b32 v61, v5, v17, s68 bitop3:0x36
	v_bitop3_b32 v60, v4, v16, s68 bitop3:0x36
	v_bitop3_b32 v59, v3, v15, s68 bitop3:0x36
	v_bitop3_b32 v58, v2, v14, s68 bitop3:0x36
	v_readlane_b32 s29, v253, 5
	s_cbranch_scc1 .LBB0_651
	v_or_b32_e32 v2, 2, v65
	v_cmp_le_i32_e32 vcc, v65, v124
	v_add_u32_e32 v5, 11, v65
	v_add_u32_e32 v4, 10, v65
	v_cndmask_b32_e32 v105, 0, v105, vcc
	v_cmp_le_i32_e32 vcc, v2, v124
	v_or_b32_e32 v2, 3, v65
	v_add_u32_e32 v3, 9, v65
	v_cndmask_b32_e32 v104, 0, v104, vcc
	v_cmp_lt_i32_e32 vcc, v65, v124
	s_nop 1
	v_cndmask_b32_e32 v106, 0, v106, vcc
	v_cmp_ge_i32_e32 vcc, v124, v2
	v_add_u32_e32 v2, 8, v65
	s_nop 0
	v_cndmask_b32_e32 v107, 0, v107, vcc
	v_cmp_le_i32_e32 vcc, v5, v124
	v_add_u32_e32 v5, 19, v65
	s_nop 0
	v_cndmask_b32_e32 v69, 0, v69, vcc
	v_cmp_le_i32_e32 vcc, v4, v124
	v_add_u32_e32 v4, 18, v65
	s_nop 0
	v_cndmask_b32_e32 v68, 0, v68, vcc
	v_cmp_le_i32_e32 vcc, v3, v124
	v_add_u32_e32 v3, 17, v65
	s_nop 0
	v_cndmask_b32_e32 v67, 0, v67, vcc
	v_cmp_le_i32_e32 vcc, v2, v124
	v_add_u32_e32 v2, 16, v65
	s_nop 0
	v_cndmask_b32_e32 v66, 0, v66, vcc
	v_cmp_le_i32_e32 vcc, v5, v124
	v_add_u32_e32 v5, 27, v65
	s_nop 0
	v_cndmask_b32_e32 v57, 0, v57, vcc
	v_cmp_le_i32_e32 vcc, v4, v124
	v_add_u32_e32 v4, 26, v65
	s_nop 0
	v_cndmask_b32_e32 v56, 0, v56, vcc
	v_cmp_le_i32_e32 vcc, v3, v124
	v_add_u32_e32 v3, 25, v65
	s_nop 0
	v_cndmask_b32_e32 v55, 0, v55, vcc
	v_cmp_le_i32_e32 vcc, v2, v124
	v_add_u32_e32 v2, 24, v65
	s_nop 0
	v_cndmask_b32_e32 v54, 0, v54, vcc
	v_cmp_le_i32_e32 vcc, v5, v124
	s_nop 1
	v_cndmask_b32_e32 v61, 0, v61, vcc
	v_cmp_le_i32_e32 vcc, v4, v124
	s_nop 1
	v_cndmask_b32_e32 v60, 0, v60, vcc
	v_cmp_le_i32_e32 vcc, v3, v124
	s_nop 1
	v_cndmask_b32_e32 v59, 0, v59, vcc
	v_cmp_le_i32_e32 vcc, v2, v124
	s_nop 1
	v_cndmask_b32_e32 v58, 0, v58, vcc
; __device__ __forceinline__ unsigned ordkey(float f) { const unsigned u = __float_as_uint(f); return u ^ ((unsigned)((int)u >> 31) | 0x80000000u); }
; __device__ __forceinline__ int crow(int r, int hi) { return (r & 3) + 8 * (r >> 2) + 4 * hi; }
; __global__ void __launch_bounds__(NWAVES * 64, 2) mega_fwd(Args args) {
;     ...
;                     for (int half = 0; half < 2; ++half) { const f16x8 kf0 = kfr[ti][half][0], kf1 = kfr[ti][half][1];
;                         fa::f32x16 sc;
; #pragma unroll
;                         for (int r = 0; r < 16; ++r) sc[r] = 0.f;
;                         sc = __builtin_amdgcn_mfma_f32_32x32x16_f16(kf0, __builtin_bit_cast(f16x8, iqL[16 * 64 + lane]), sc, 0, 0, 0);
;                         sc = __builtin_amdgcn_mfma_f32_32x32x16_f16(kf1, __builtin_bit_cast(f16x8, iqL[17 * 64 + lane]), sc, 0, 0, 0);
; #pragma unroll 2
;                         for (int h = 0; h < 8; ++h) { fa::f32x16 a;
; #pragma unroll
;                             for (int r = 0; r < 16; ++r) a[r] = 0.f;
;                             a = __builtin_amdgcn_mfma_f32_32x32x16_f16(kf0, __builtin_bit_cast(f16x8, iqL[(2 * h) * 64 + lane]), a, 0, 0, 0);
;                             a = __builtin_amdgcn_mfma_f32_32x32x16_f16(kf1, __builtin_bit_cast(f16x8, iqL[(2 * h + 1) * 64 + lane]), a, 0, 0, 0);
;                             const float sg = ((sgnbits >> h) & 1u) ? -1.f : 1.f;
; #pragma unroll
;                             for (int r = 0; r < 16; ++r) sc[r] = __builtin_fmaf(__builtin_fabsf(a[r]), sg, sc[r]); }
; #pragma unroll
;                         for (int r = 0; r < 16; ++r) keys[ti][16 * half + r] = ordkey(sc[r]);
;                         if (k0 + 63 > 32 * qg) {
; #pragma unroll
;                             for (int r = 0; r < 16; ++r) { const int kidx = k0 + 32 * half + fa::crow(r, hi); keys[ti][16 * half + r] = (kidx <= t) ? keys[ti][16 * half + r] : 0u; } } }
.LBB0_651:
	v_mfma_f32_32x32x16_f16 v[2:17], v[38:41], v[100:103], 0
	s_mov_b32 s26, 0
	v_mfma_f32_32x32x16_f16 v[2:17], v[34:37], v[70:73], v[2:17]
	ds_read_b128 v[172:175], v141
	ds_read_b128 v[196:199], v141 offset:1024
	ds_read_b128 v[224:227], v141 offset:2048
	ds_read_b128 v[176:179], v141 offset:3072
.LBB0_652:
	s_waitcnt lgkmcnt(3)
	v_mfma_f32_32x32x16_f16 v[18:33], v[38:41], v[172:175], 0
	s_waitcnt lgkmcnt(2)
	v_mfma_f32_32x32x16_f16 v[18:33], v[34:37], v[196:199], v[18:33]
	s_waitcnt lgkmcnt(1)
	v_mfma_f32_32x32x16_f16 v[208:223], v[38:41], v[224:227], 0
	s_waitcnt lgkmcnt(0)
	v_mfma_f32_32x32x16_f16 v[208:223], v[34:37], v[176:179], v[208:223]
	v_add_u32_e32 v141, 0x1000, v141
	ds_read_b128 v[172:175], v141
	ds_read_b128 v[196:199], v141 offset:1024
	ds_read_b128 v[224:227], v141 offset:2048
	ds_read_b128 v[176:179], v141 offset:3072
	v_bfe_u32 v70, v140, s26, 1
	v_cmp_eq_u32_e32 vcc, 0, v70
	v_lshrrev_b32_e32 v180, s26, v140
	v_and_b32_e32 v180, 2, v180
	v_cndmask_b32_e64 v70, -1.0, 1.0, vcc
	v_cmp_eq_u32_e32 vcc, 0, v180
	s_add_i32 s26, s26, 2
	v_cndmask_b32_e64 v180, -1.0, 1.0, vcc
	s_cmp_lg_u32 s26, 8
	v_fma_f32 v72, |v18|, v70, v2
	v_fma_f32 v73, |v19|, v70, v3
	v_fma_f32 v100, |v20|, v70, v4
	v_fma_f32 v101, |v21|, v70, v5
	v_fma_f32 v22, |v22|, v70, v6
	v_fma_f32 v23, |v23|, v70, v7
	v_fma_f32 v24, |v24|, v70, v8
	v_fma_f32 v25, |v25|, v70, v9
	v_fma_f32 v26, |v26|, v70, v10
	v_fma_f32 v27, |v27|, v70, v11
	v_fma_f32 v28, |v28|, v70, v12
	v_fma_f32 v29, |v29|, v70, v13
	v_fma_f32 v30, |v30|, v70, v14
	v_fma_f32 v31, |v31|, v70, v15
	v_fma_f32 v32, |v32|, v70, v16
	v_fma_f32 v33, |v33|, v70, v17
	v_fma_f32 v4, |v210|, v180, v100
	v_fma_f32 v5, |v211|, v180, v101
	v_fma_f32 v2, |v208|, v180, v72
	v_fma_f32 v3, |v209|, v180, v73
	v_fma_f32 v8, |v214|, v180, v24
	v_fma_f32 v9, |v215|, v180, v25
	v_fma_f32 v6, |v212|, v180, v22
	v_fma_f32 v7, |v213|, v180, v23
	v_fma_f32 v12, |v218|, v180, v28
	v_fma_f32 v13, |v219|, v180, v29
	v_fma_f32 v10, |v216|, v180, v26
	v_fma_f32 v11, |v217|, v180, v27
	v_fma_f32 v16, |v222|, v180, v32
	v_fma_f32 v17, |v223|, v180, v33
	v_fma_f32 v14, |v220|, v180, v30
	v_fma_f32 v15, |v221|, v180, v31
	s_cbranch_scc1 .LBB0_652
	s_waitcnt lgkmcnt(0)
	v_ashrrev_i32_e32 v18, 31, v2
	v_ashrrev_i32_e32 v19, 31, v3
	v_ashrrev_i32_e32 v20, 31, v4
	v_ashrrev_i32_e32 v21, 31, v5
	v_bitop3_b32 v21, v21, v5, s68 bitop3:0x36
	v_bitop3_b32 v25, v20, v4, s68 bitop3:0x36
	v_bitop3_b32 v23, v19, v3, s68 bitop3:0x36
	v_bitop3_b32 v26, v18, v2, s68 bitop3:0x36
	v_ashrrev_i32_e32 v2, 31, v6
	v_ashrrev_i32_e32 v3, 31, v7
	v_ashrrev_i32_e32 v4, 31, v8
	v_ashrrev_i32_e32 v5, 31, v9
	v_bitop3_b32 v18, v5, v9, s68 bitop3:0x36
	v_bitop3_b32 v20, v4, v8, s68 bitop3:0x36
	v_bitop3_b32 v24, v3, v7, s68 bitop3:0x36
	v_bitop3_b32 v22, v2, v6, s68 bitop3:0x36
	v_ashrrev_i32_e32 v2, 31, v10
	v_ashrrev_i32_e32 v3, 31, v11
	v_ashrrev_i32_e32 v4, 31, v12
	v_ashrrev_i32_e32 v5, 31, v13
	v_bitop3_b32 v13, v5, v13, s68 bitop3:0x36
	v_bitop3_b32 v9, v4, v12, s68 bitop3:0x36
	v_bitop3_b32 v11, v3, v11, s68 bitop3:0x36
	v_bitop3_b32 v19, v2, v10, s68 bitop3:0x36
	v_ashrrev_i32_e32 v3, 31, v14
	v_ashrrev_i32_e32 v4, 31, v15
	v_ashrrev_i32_e32 v5, 31, v16
	v_ashrrev_i32_e32 v2, 31, v17
	v_bitop3_b32 v2, v2, v17, s68 bitop3:0x36
	v_bitop3_b32 v8, v5, v16, s68 bitop3:0x36
	v_bitop3_b32 v10, v4, v15, s68 bitop3:0x36
	s_andn2_b64 vcc, exec, s[40:41]
	v_bitop3_b32 v12, v3, v14, s68 bitop3:0x36
	s_cbranch_vccnz .LBB0_659
	v_add_u32_e32 v3, 32, v65
	v_or_b32_e32 v5, 2, v3
	v_or_b32_e32 v4, 3, v3
	v_cmp_le_i32_e32 vcc, v5, v124
	v_add_u32_e32 v6, 40, v65
	v_add_u32_e32 v5, 41, v65
	v_cndmask_b32_e32 v25, 0, v25, vcc
	v_cmp_le_i32_e32 vcc, v4, v124
	v_add_u32_e32 v4, 42, v65
	s_nop 0
	v_cndmask_b32_e32 v21, 0, v21, vcc
	v_cmp_le_i32_e32 vcc, v3, v124
	s_nop 1
	v_cndmask_b32_e32 v26, 0, v26, vcc
	v_cmp_gt_i32_e32 vcc, v124, v3
	v_add_u32_e32 v3, 43, v65
	s_nop 0
	v_cndmask_b32_e32 v23, 0, v23, vcc
	v_cmp_le_i32_e32 vcc, v6, v124
	v_add_u32_e32 v6, 48, v65
	s_nop 0
	v_cndmask_b32_e32 v22, 0, v22, vcc
	v_cmp_le_i32_e32 vcc, v5, v124
	v_add_u32_e32 v5, 49, v65
	s_nop 0
	v_cndmask_b32_e32 v24, 0, v24, vcc
	v_cmp_le_i32_e32 vcc, v4, v124
	v_add_u32_e32 v4, 50, v65
	s_nop 0
	v_cndmask_b32_e32 v20, 0, v20, vcc
	v_cmp_le_i32_e32 vcc, v3, v124
	v_add_u32_e32 v3, 51, v65
	s_nop 0
	v_cndmask_b32_e32 v18, 0, v18, vcc
	v_cmp_le_i32_e32 vcc, v6, v124
	v_add_u32_e32 v6, 56, v65
	s_nop 0
	v_cndmask_b32_e32 v19, 0, v19, vcc
	v_cmp_le_i32_e32 vcc, v5, v124
	v_add_u32_e32 v5, 57, v65
	s_nop 0
	v_cndmask_b32_e32 v11, 0, v11, vcc
	v_cmp_le_i32_e32 vcc, v4, v124
	v_add_u32_e32 v4, 58, v65
	s_nop 0
	v_cndmask_b32_e32 v9, 0, v9, vcc
	v_cmp_le_i32_e32 vcc, v3, v124
	v_add_u32_e32 v3, 59, v65
	s_nop 0
	v_cndmask_b32_e32 v13, 0, v13, vcc
	v_cmp_le_i32_e32 vcc, v6, v124
	s_nop 1
	v_cndmask_b32_e32 v12, 0, v12, vcc
	v_cmp_le_i32_e32 vcc, v5, v124
	s_nop 1
	v_cndmask_b32_e32 v10, 0, v10, vcc
	v_cmp_le_i32_e32 vcc, v4, v124
	s_nop 1
	v_cndmask_b32_e32 v8, 0, v8, vcc
	v_cmp_le_i32_e32 vcc, v3, v124
	s_nop 1
	v_cndmask_b32_e32 v2, 0, v2, vcc
	s_branch .LBB0_659
